# v5: + normf g/sh/sc hoisted out of the tile bodies, prologue weight loads nt, norm<0> hoist + next-row x prefetch
# speedup vs baseline: 1.0120x; 1.0120x over previous
.LBB0_31:
	s_lshl_b32 s8, s22, 6
	s_ashr_i32 s9, s8, 31
	s_mul_i32 s9, s9, s3
	s_mul_hi_u32 s15, s8, s3
	s_add_i32 s9, s15, s9
	s_mul_i32 s8, s8, s3
	s_lshl_b32 s16, s23, 5
	s_ashr_i32 s17, s16, 31
	s_lshl_b64 s[8:9], s[8:9], 2
	s_add_u32 s8, s6, s8
	s_addc_u32 s9, s7, s9
	s_lshl_b64 s[6:7], s[16:17], 2
	s_add_u32 s6, s8, s6
	v_lshlrev_b32_e32 v0, 4, v64
	s_addc_u32 s7, s9, s7
	v_and_b32_e32 v0, 0x70, v0
	v_mov_b32_e32 v1, 0
	v_lshrrev_b32_e32 v8, 3, v64
	v_lshl_add_u64 v[2:3], s[6:7], 0, v[0:1]
	s_lshl_b32 s6, s3, 3
	v_mul_u32_u24_e32 v0, s3, v8
	s_ashr_i32 s7, s6, 31
	v_lshlrev_b32_e32 v0, 2, v0
	s_lshl_b64 s[8:9], s[6:7], 2
	s_add_i32 s7, s6, s6
	v_lshl_add_u64 v[4:5], v[2:3], 0, v[0:1]
	s_add_i32 s7, s7, s7
	v_lshl_add_u64 v[6:7], v[4:5], 0, s[8:9]
	v_mov_b32_e32 v0, s7
	global_load_dwordx4 v[60:63], v[4:5], off nt
	global_load_dwordx4 v[56:59], v[6:7], off nt
	v_lshl_add_u64 v[4:5], v[6:7], 0, s[8:9]
	v_mad_u32_u24 v0, s3, v8, v0
	v_lshl_add_u64 v[6:7], v[4:5], 0, s[8:9]
	global_load_dwordx4 v[52:55], v[4:5], off nt
	global_load_dwordx4 v[48:51], v[6:7], off nt
	v_lshl_add_u64 v[4:5], v[0:1], 2, v[2:3]
	v_add_u32_e32 v0, s6, v0
	v_lshl_add_u64 v[6:7], v[0:1], 2, v[2:3]
	v_add_u32_e32 v0, s6, v0
	global_load_dwordx4 v[44:47], v[4:5], off nt
	global_load_dwordx4 v[40:43], v[6:7], off nt
	v_lshl_add_u64 v[4:5], v[0:1], 2, v[2:3]
	v_add_u32_e32 v0, s6, v0
	v_lshl_add_u64 v[0:1], v[0:1], 2, v[2:3]
	global_load_dwordx4 v[36:39], v[4:5], off nt
	global_load_dwordx4 v[32:35], v[0:1], off nt

.LBB0_55:
	s_lshl_b32 s14, s22, 6
	s_ashr_i32 s15, s14, 31
	s_mul_i32 s15, s15, s18
	s_mul_hi_u32 s19, s14, s18
	s_add_i32 s15, s19, s15
	s_mul_i32 s14, s14, s18
	s_lshl_b32 s20, s23, 5
	s_ashr_i32 s21, s20, 31
	s_lshl_b64 s[14:15], s[14:15], 2
	s_add_u32 s14, s8, s14
	s_addc_u32 s15, s9, s15
	s_lshl_b64 s[8:9], s[20:21], 2
	s_add_u32 s8, s14, s8
	s_addc_u32 s9, s15, s9
	v_lshl_add_u64 v[24:25], s[8:9], 0, v[68:69]
	v_mul_u32_u24_e32 v0, s18, v65
	s_lshl_b32 s8, s18, 3
	v_lshlrev_b32_e32 v0, 2, v0
	v_mov_b32_e32 v1, v69
	s_ashr_i32 s9, s8, 31
	v_lshl_add_u64 v[8:9], v[24:25], 0, v[0:1]
	s_lshl_b64 s[14:15], s[8:9], 2
	v_lshl_add_u64 v[10:11], v[8:9], 0, s[14:15]
	s_add_i32 s9, s8, s8
	v_lshl_add_u64 v[16:17], v[10:11], 0, s[14:15]
	s_add_i32 s9, s9, s9
	global_load_dwordx4 v[4:7], v[8:9], off nt
	global_load_dwordx4 v[0:3], v[10:11], off nt
	v_lshl_add_u64 v[18:19], v[16:17], 0, s[14:15]
	global_load_dwordx4 v[12:15], v[16:17], off nt
	global_load_dwordx4 v[8:11], v[18:19], off nt
	v_mov_b32_e32 v16, s9
	v_mad_u32_u24 v16, s18, v65, v16
	v_mov_b32_e32 v17, v69
	v_lshl_add_u64 v[26:27], v[16:17], 2, v[24:25]
	v_add_u32_e32 v28, s8, v16
	v_mov_b32_e32 v29, v69
	v_lshl_add_u64 v[30:31], v[28:29], 2, v[24:25]
	global_load_dwordx4 v[20:23], v[26:27], off nt
	global_load_dwordx4 v[16:19], v[30:31], off nt
	v_add_u32_e32 v26, s8, v28
	v_mov_b32_e32 v27, v69
	v_lshl_add_u64 v[80:81], v[26:27], 2, v[24:25]
	v_add_u32_e32 v26, s8, v26
	v_lshl_add_u64 v[82:83], v[26:27], 2, v[24:25]
	global_load_dwordx4 v[28:31], v[80:81], off nt
	global_load_dwordx4 v[24:27], v[82:83], off nt

.LBB0_477:
	s_mov_b32 s12, 0
	s_ashr_i32 s4, s10, 13
	s_mulk_i32 s4, 0x1800
	s_ashr_i32 s5, s4, 31
	s_lshl_b64 s[2:3], s[4:5], 2
	s_add_u32 s2, s8, s2
	s_addc_u32 s3, s9, s3
	s_add_u32 s4, s2, 0x1000
	s_addc_u32 s5, s3, 0
	global_load_dwordx4 v[130:133], v[4:5], off
	global_load_dwordx4 v[134:137], v[4:5], off offset:1024
	global_load_dwordx4 v[138:141], v[4:5], off offset:2048
	global_load_dwordx4 v[142:145], v[4:5], off offset:3072
	global_load_dwordx4 v[146:149], v0, s[2:3]
	global_load_dwordx4 v[150:153], v0, s[2:3] offset:1024
	global_load_dwordx4 v[154:157], v0, s[2:3] offset:2048
	global_load_dwordx4 v[158:161], v0, s[2:3] offset:3072
	global_load_dwordx4 v[162:165], v0, s[4:5]
	global_load_dwordx4 v[166:169], v9, s[4:5]
	global_load_dwordx4 v[170:173], v10, s[4:5]
	global_load_dwordx4 v[174:177], v11, s[4:5]
	s_mov_b32 s6, s10
	s_ashr_i32 s7, s6, 31
	s_lshl_b64 s[2:3], s[6:7], 12
	v_lshl_add_u64 v[194:195], v[2:3], 0, s[2:3]
	global_load_dwordx4 v[178:181], v[194:195], off
	global_load_dwordx4 v[182:185], v[194:195], off offset:1024
	global_load_dwordx4 v[186:189], v[194:195], off offset:2048
	global_load_dwordx4 v[190:193], v[194:195], off offset:3072
	s_waitcnt vmcnt(0)
.LBB0_478:
	s_add_i32 s6, s10, s12
	s_ashr_i32 s7, s6, 31
	s_lshl_b64 s[6:7], s[6:7], 10
	v_mov_b32_e32 v53, 0
	s_waitcnt vmcnt(4)
	v_lshl_add_u64 v[40:41], v[6:7], 0, s[6:7]
	s_add_i32 s12, s12, 1
	s_cmp_eq_u32 s12, 16
	s_cselect_b32 s2, 0, 0x1000
	s_mov_b32 s3, 0
	v_mov_b64_e32 v[16:17], v[178:179]
	v_mov_b64_e32 v[18:19], v[180:181]
	v_mov_b64_e32 v[20:21], v[182:183]
	v_mov_b64_e32 v[22:23], v[184:185]
	v_mov_b64_e32 v[28:29], v[186:187]
	v_mov_b64_e32 v[30:31], v[188:189]
	v_mov_b64_e32 v[24:25], v[190:191]
	v_mov_b64_e32 v[26:27], v[192:193]
	v_mov_b64_e32 v[12:13], v[130:131]
	v_mov_b64_e32 v[14:15], v[132:133]
	v_mov_b64_e32 v[32:33], v[146:147]
	v_mov_b64_e32 v[34:35], v[148:149]
	v_mov_b64_e32 v[36:37], v[162:163]
	v_mov_b64_e32 v[38:39], v[164:165]
	v_lshl_add_u64 v[194:195], v[194:195], 0, s[2:3]
	global_load_dwordx4 v[178:181], v[194:195], off
	global_load_dwordx4 v[182:185], v[194:195], off offset:1024
	global_load_dwordx4 v[186:189], v[194:195], off offset:2048
	global_load_dwordx4 v[190:193], v[194:195], off offset:3072
	v_pk_mul_f32 v[42:43], v[18:19], v[18:19]
	v_pk_mul_f32 v[44:45], v[16:17], v[16:17]
	s_nop 0
	v_pk_mul_f32 v[46:47], v[22:23], v[22:23]
	v_pk_mul_f32 v[48:49], v[20:21], v[20:21]
	v_pk_mov_b32 v[54:55], v[44:45], v[42:43] op_sel:[1,0]
	v_mov_b32_e32 v45, v43
	v_pk_mov_b32 v[42:43], v[48:49], v[46:47] op_sel:[1,0]
	v_mov_b32_e32 v49, v47
	s_nop 0
	v_mul_f32_e32 v50, v29, v29
	v_mul_f32_e32 v52, v31, v31
	v_pk_add_f32 v[44:45], v[54:55], v[44:45]
	v_pk_add_f32 v[42:43], v[42:43], v[48:49]
	v_mul_f32_e32 v56, v24, v24
	v_mul_f32_e32 v57, v25, v25
	v_mul_f32_e32 v58, v26, v26
	v_mul_f32_e32 v59, v27, v27
	v_pk_fma_f32 v[46:47], v[28:29], v[28:29], v[50:51] op_sel_hi:[1,1,0]
	v_pk_fma_f32 v[50:51], v[30:31], v[30:31], v[52:53] op_sel_hi:[1,1,0]
	v_pk_add_f32 v[44:45], v[44:45], v[44:45] op_sel:[0,1] op_sel_hi:[1,0]
	v_pk_add_f32 v[42:43], v[42:43], v[42:43] op_sel:[0,1] op_sel_hi:[1,0]
	v_mov_b32_e32 v47, v58
	v_mov_b32_e32 v51, v59
	v_mov_b32_e32 v45, v56
	v_mov_b32_e32 v43, v57
	v_pk_add_f32 v[46:47], v[46:47], v[50:51]
	v_pk_add_f32 v[42:43], v[44:45], v[42:43]
	s_nop 0
	v_pk_add_f32 v[36:37], v[36:37], 1.0 op_sel_hi:[1,0]
	v_pk_add_f32 v[42:43], v[42:43], v[46:47]
	v_pk_add_f32 v[38:39], v[38:39], 1.0 op_sel_hi:[1,0]
	v_add_f32_e32 v42, v42, v43
	s_nop 1
	v_add_f32_dpp v42, v42, v42 quad_perm:[1,0,3,2] row_mask:0xf bank_mask:0xf bound_ctrl:1
	s_nop 1
	v_add_f32_dpp v42, v42, v42 quad_perm:[2,3,0,1] row_mask:0xf bank_mask:0xf bound_ctrl:1
	s_nop 1
	v_add_f32_dpp v42, v42, v42 row_half_mirror row_mask:0xf bank_mask:0xf bound_ctrl:1
	s_nop 1
	v_add_f32_dpp v42, v42, v42 row_mirror row_mask:0xf bank_mask:0xf bound_ctrl:1
	ds_swizzle_b32 v43, v42 offset:swizzle(SWAP,16)
	s_waitcnt lgkmcnt(0)
	v_add_f32_e32 v42, v42, v43
	ds_bpermute_b32 v43, v8, v42
	s_waitcnt lgkmcnt(0)
	v_add_f32_e32 v42, v42, v43
	v_fmamk_f32 v42, v42, 0x3a800000, v254
	v_rsq_f32_e32 v42, v42
	s_nop 0
	v_pk_mul_f32 v[16:17], v[16:17], v[42:43] op_sel_hi:[1,0]
	s_nop 0
	v_pk_mul_f32 v[12:13], v[12:13], v[16:17]
	v_pk_mul_f32 v[18:19], v[18:19], v[42:43] op_sel_hi:[1,0]
	v_pk_fma_f32 v[12:13], v[36:37], v[12:13], v[32:33]
	v_pk_mul_f32 v[14:15], v[14:15], v[18:19]
	v_cvt_pk_fp8_f32 v53, v12, v13
	v_pk_fma_f32 v[14:15], v[38:39], v[14:15], v[34:35]
	v_pk_mul_f32 v[20:21], v[20:21], v[42:43] op_sel_hi:[1,0]
	v_mov_b32_e32 v36, 0
	v_cvt_pk_fp8_f32 v53, v14, v15 op_sel:[0,0,1]
	v_pk_mul_f32 v[22:23], v[22:23], v[42:43] op_sel_hi:[1,0]
	v_pk_mul_f32 v[28:29], v[28:29], v[42:43] op_sel_hi:[1,0]
	v_pk_mul_f32 v[30:31], v[30:31], v[42:43] op_sel_hi:[1,0]
	global_store_dword v[40:41], v53, off
	v_mov_b64_e32 v[12:13], v[134:135]
	v_mov_b64_e32 v[14:15], v[136:137]
	v_mov_b64_e32 v[16:17], v[166:167]
	v_mov_b64_e32 v[18:19], v[168:169]
	v_mov_b64_e32 v[32:33], v[150:151]
	v_mov_b64_e32 v[34:35], v[152:153]
	v_pk_mul_f32 v[24:25], v[24:25], v[42:43] op_sel_hi:[1,0]
	v_pk_mul_f32 v[26:27], v[26:27], v[42:43] op_sel_hi:[1,0]
	s_nop 0
	v_pk_mul_f32 v[12:13], v[12:13], v[20:21]
	s_nop 0
	v_pk_add_f32 v[16:17], v[16:17], 1.0 op_sel_hi:[1,0]
	v_pk_mul_f32 v[14:15], v[14:15], v[22:23]
	s_nop 0
	v_pk_fma_f32 v[12:13], v[16:17], v[12:13], v[32:33]
	v_pk_add_f32 v[18:19], v[18:19], 1.0 op_sel_hi:[1,0]
	v_cvt_pk_fp8_f32 v36, v12, v13
	v_pk_fma_f32 v[14:15], v[18:19], v[14:15], v[34:35]
	v_mov_b32_e32 v32, 0
	v_cvt_pk_fp8_f32 v36, v14, v15 op_sel:[0,0,1]
	global_store_dword v[40:41], v36, off offset:256
	v_mov_b64_e32 v[12:13], v[138:139]
	v_mov_b64_e32 v[14:15], v[140:141]
	v_mov_b64_e32 v[16:17], v[170:171]
	v_mov_b64_e32 v[18:19], v[172:173]
	v_mov_b64_e32 v[20:21], v[154:155]
	v_mov_b64_e32 v[22:23], v[156:157]
	s_nop 0
	v_pk_mul_f32 v[12:13], v[28:29], v[12:13]
	s_nop 0
	v_pk_add_f32 v[16:17], v[16:17], 1.0 op_sel_hi:[1,0]
	v_pk_mul_f32 v[14:15], v[30:31], v[14:15]
	s_nop 0
	v_pk_fma_f32 v[12:13], v[12:13], v[16:17], v[20:21]
	v_mov_b32_e32 v28, 0
	v_cvt_pk_fp8_f32 v32, v12, v13
	v_pk_add_f32 v[12:13], v[18:19], 1.0 op_sel_hi:[1,0]
	s_nop 0
	v_pk_fma_f32 v[12:13], v[14:15], v[12:13], v[22:23]
	s_nop 0
	v_cvt_pk_fp8_f32 v32, v12, v13 op_sel:[0,0,1]
	global_store_dword v[40:41], v32, off offset:512
	v_mov_b64_e32 v[12:13], v[142:143]
	v_mov_b64_e32 v[14:15], v[144:145]
	v_mov_b64_e32 v[16:17], v[174:175]
	v_mov_b64_e32 v[18:19], v[176:177]
	v_mov_b64_e32 v[20:21], v[158:159]
	v_mov_b64_e32 v[22:23], v[160:161]
	s_nop 0
	v_pk_mul_f32 v[12:13], v[24:25], v[12:13]
	s_nop 0
	v_pk_add_f32 v[16:17], v[16:17], 1.0 op_sel_hi:[1,0]
	s_nop 0
	v_pk_fma_f32 v[12:13], v[12:13], v[16:17], v[20:21]
	s_nop 0
	v_cvt_pk_fp8_f32 v28, v12, v13
	v_pk_mul_f32 v[12:13], v[26:27], v[14:15]
	v_pk_add_f32 v[14:15], v[18:19], 1.0 op_sel_hi:[1,0]
	s_nop 0
	v_pk_fma_f32 v[12:13], v[12:13], v[14:15], v[22:23]
	s_nop 0
	v_cvt_pk_fp8_f32 v28, v12, v13 op_sel:[0,0,1]
	global_store_dword v[40:41], v28, off offset:768
	s_cbranch_scc0 .LBB0_478
	s_add_i32 s1, s1, s0
	s_add_i32 s10, s10, s11
	s_cmpk_gt_i32 s1, 0xff
	s_cbranch_scc0 .LBB0_477

.LBB0_1053:
	s_barrier
	s_and_saveexec_b64 s[12:13], s[2:3]
	ds_write_b32 v166, v1
	s_or_b64 exec, exec, s[12:13]
	s_ashr_i32 s0, s41, 6
	s_add_i32 s0, s0, s44
	s_lshl_b32 s49, s41, 7
	s_mul_hi_i32 s1, s0, 0x6000
	s_mulk_i32 s0, 0x6000
	s_add_u32 s12, s16, s0
	s_addc_u32 s13, s17, s1
	s_add_i32 s26, s49, s45
	s_ashr_i32 s27, s26, 31
	s_lshl_b64 s[0:1], s[26:27], 11
	v_lshl_add_u64 v[66:67], v[80:81], 0, s[0:1]
	s_or_b32 s0, s26, 1
	s_ashr_i32 s1, s0, 31
	s_lshl_b64 s[0:1], s[0:1], 11
	v_lshl_add_u64 v[68:69], v[80:81], 0, s[0:1]
	global_load_dwordx2 v[118:119], v[66:67], off
	global_load_dwordx2 v[114:115], v[66:67], off offset:512
	global_load_dwordx2 v[110:111], v[66:67], off offset:1024
	global_load_dwordx2 v[120:121], v[66:67], off offset:1536
	s_nop 0
	global_load_dwordx2 v[66:67], v[68:69], off
	global_load_dwordx2 v[116:117], v[68:69], off offset:512
	global_load_dwordx2 v[112:113], v[68:69], off offset:1024
	global_load_dwordx2 v[122:123], v[68:69], off offset:1536
	s_add_u32 s0, s12, 0x103000
	s_addc_u32 s1, s13, 0
	s_add_u32 s12, s12, 0x104000
	s_addc_u32 s13, s13, 0
	v_mov_b32_e32 v89, v1
	v_mov_b32_e32 v91, v1
	v_mov_b32_e32 v93, v1
	v_lshl_add_u64 v[108:109], s[0:1], 0, v[0:1]
	v_lshl_add_u64 v[106:107], s[12:13], 0, v[0:1]
	v_lshl_add_u64 v[104:105], s[0:1], 0, v[88:89]
	v_lshl_add_u64 v[102:103], s[12:13], 0, v[88:89]
	v_lshl_add_u64 v[100:101], s[0:1], 0, v[90:91]
	v_lshl_add_u64 v[98:99], s[12:13], 0, v[90:91]
	v_lshl_add_u64 v[94:95], s[0:1], 0, v[92:93]
	v_lshl_add_u64 v[96:97], s[12:13], 0, v[92:93]
	global_load_dwordx4 v[192:195], v[84:85], off
	global_load_dwordx4 v[196:199], v[84:85], off offset:1024
	global_load_dwordx4 v[200:203], v[84:85], off offset:2048
	global_load_dwordx4 v[204:207], v[84:85], off offset:3072
	global_load_dwordx4 v[208:211], v[108:109], off
	global_load_dwordx4 v[212:215], v[106:107], off
	global_load_dwordx4 v[216:219], v[104:105], off
	global_load_dwordx4 v[220:223], v[102:103], off
	global_load_dwordx4 v[224:227], v[100:101], off
	global_load_dwordx4 v[228:231], v[98:99], off
	global_load_dwordx4 v[232:235], v[94:95], off
	global_load_dwordx4 v[236:239], v[96:97], off
	s_waitcnt vmcnt(0)
	s_mov_b32 s0, 0
	v_mov_b32_e32 v124, v176
	v_mov_b32_e32 v89, v175
.LBB0_1056:
	s_nop 0
	v_and_b32_e32 v159, 0xffff0000, v67
	v_and_b32_e32 v158, 0xffff0000, v66
	v_mov_b64_e32 v[72:73], v[118:119]
	v_mov_b64_e32 v[74:75], v[114:115]
	v_lshlrev_b32_e32 v157, 16, v67
	v_lshlrev_b32_e32 v156, 16, v66
	v_pk_mul_f32 v[66:67], v[158:159], v[158:159]
	v_mov_b64_e32 v[76:77], v[110:111]
	v_and_b32_e32 v163, 0xffff0000, v73
	v_and_b32_e32 v162, 0xffff0000, v72
	v_pk_fma_f32 v[66:67], v[156:157], v[156:157], v[66:67]
	v_and_b32_e32 v155, 0xffff0000, v75
	v_and_b32_e32 v154, 0xffff0000, v74
	v_lshlrev_b32_e32 v142, 16, v76
	v_and_b32_e32 v143, 0xffff0000, v76
	v_lshlrev_b32_e32 v132, 16, v120
	v_lshlrev_b32_e32 v161, 16, v73
	v_lshlrev_b32_e32 v160, 16, v72
	v_pk_mul_f32 v[72:73], v[162:163], v[162:163]
	v_pk_add_f32 v[66:67], v[66:67], v[66:67] op_sel_hi:[0,1]
	v_lshlrev_b32_e32 v153, 16, v75
	v_lshlrev_b32_e32 v152, 16, v74
	v_pk_mul_f32 v[74:75], v[154:155], v[154:155]
	v_lshlrev_b32_e32 v146, 16, v77
	s_nop 0
	v_mov_b64_e32 v[68:69], v[116:117]
	v_pk_fma_f32 v[72:73], v[160:161], v[160:161], v[72:73]
	v_pk_fma_f32 v[74:75], v[152:153], v[152:153], v[74:75]
	v_mul_f32_e32 v133, v142, v142
	v_mul_f32_e32 v139, v143, v143
	v_and_b32_e32 v147, 0xffff0000, v77
	v_mul_f32_e32 v66, v146, v146
	v_mov_b32_e32 v138, v132
	s_nop 0
	v_mov_b64_e32 v[70:71], v[112:113]
	v_and_b32_e32 v125, 0xffff0000, v120
	v_lshlrev_b32_e32 v134, 16, v121
	v_and_b32_e32 v135, 0xffff0000, v121
	v_pk_add_f32 v[72:73], v[72:73], v[72:73] op_sel_hi:[0,1]
	v_pk_add_f32 v[74:75], v[74:75], v[74:75] op_sel_hi:[0,1]
	v_and_b32_e32 v151, 0xffff0000, v69
	v_and_b32_e32 v150, 0xffff0000, v68
	v_pk_fma_f32 v[76:77], v[146:147], v[146:147], v[66:67] op_sel_hi:[1,1,0]
	v_pk_add_f32 v[138:139], v[132:133], v[138:139]
	v_lshlrev_b32_e32 v136, 16, v70
	v_and_b32_e32 v137, 0xffff0000, v70
	s_nop 0
	v_lshlrev_b32_e32 v128, 16, v122
	v_lshlrev_b32_e32 v149, 16, v69
	v_lshlrev_b32_e32 v148, 16, v68
	v_pk_mul_f32 v[68:69], v[150:151], v[150:151]
	v_lshlrev_b32_e32 v144, 16, v71
	v_mul_f32_e32 v76, v125, v125
	v_mul_f32_e32 v74, v134, v134
	v_mul_f32_e32 v72, v135, v135
	v_mul_f32_e32 v178, v132, v132
	v_mov_b32_e32 v179, v139
	v_pk_fma_f32 v[68:69], v[148:149], v[148:149], v[68:69]
	v_mul_f32_e32 v129, v136, v136
	v_mul_f32_e32 v141, v137, v137
	v_and_b32_e32 v145, 0xffff0000, v71
	v_mul_f32_e32 v66, v144, v144
	v_pk_add_f32 v[76:77], v[178:179], v[76:77]
	v_pk_add_f32 v[72:73], v[74:75], v[72:73]
	v_mov_b32_e32 v140, v128
	s_waitcnt lgkmcnt(0)
	v_and_b32_e32 v93, 0xffff0000, v122
	v_lshlrev_b32_e32 v130, 16, v123
	v_and_b32_e32 v131, 0xffff0000, v123
	v_pk_add_f32 v[68:69], v[68:69], v[68:69] op_sel_hi:[0,1]
	v_pk_fma_f32 v[70:71], v[144:145], v[144:145], v[66:67] op_sel_hi:[1,1,0]
	v_pk_add_f32 v[72:73], v[76:77], v[72:73]
	v_pk_add_f32 v[74:75], v[128:129], v[140:141]
	v_add_f32_e32 v76, v72, v73
	v_mul_f32_e32 v70, v93, v93
	v_mul_f32_e32 v68, v130, v130
	v_mul_f32_e32 v66, v131, v131
	v_mul_f32_e32 v72, v128, v128
	v_mov_b32_e32 v73, v75
	v_pk_add_f32 v[70:71], v[72:73], v[70:71]
	v_pk_add_f32 v[66:67], v[68:69], v[66:67]
	s_add_i32 s12, s15, s0
	v_pk_add_f32 v[66:67], v[70:71], v[66:67]
	s_add_i32 s28, s12, 16
	v_add_f32_e32 v66, v66, v67
	v_add_f32_dpp v67, v76, v76 quad_perm:[1,0,3,2] row_mask:0xf bank_mask:0xf bound_ctrl:1
	s_ashr_i32 s29, s28, 31
	v_add_f32_dpp v66, v66, v66 quad_perm:[1,0,3,2] row_mask:0xf bank_mask:0xf bound_ctrl:1
	v_add_f32_dpp v67, v67, v67 quad_perm:[2,3,0,1] row_mask:0xf bank_mask:0xf bound_ctrl:1
	s_lshl_b64 s[28:29], s[28:29], 11
	v_add_f32_dpp v66, v66, v66 quad_perm:[2,3,0,1] row_mask:0xf bank_mask:0xf bound_ctrl:1
	v_add_f32_dpp v67, v67, v67 row_half_mirror row_mask:0xf bank_mask:0xf bound_ctrl:1
	v_lshl_add_u64 v[120:121], v[80:81], 0, s[28:29]
	v_add_f32_dpp v66, v66, v66 row_half_mirror row_mask:0xf bank_mask:0xf bound_ctrl:1
	v_add_f32_dpp v67, v67, v67 row_mirror row_mask:0xf bank_mask:0xf bound_ctrl:1
	ds_swizzle_b32 v68, v67 offset:swizzle(SWAP,16)
	v_add_f32_dpp v66, v66, v66 row_mirror row_mask:0xf bank_mask:0xf bound_ctrl:1
	s_add_i32 s28, s12, 17
	s_ashr_i32 s29, s28, 31
	s_lshl_b64 s[28:29], s[28:29], 11
	s_waitcnt lgkmcnt(0)
	v_add_f32_e32 v67, v67, v68
	ds_bpermute_b32 v68, v79, v67
	v_lshl_add_u64 v[122:123], v[80:81], 0, s[28:29]
	global_load_dwordx2 v[118:119], v[120:121], off
	global_load_dwordx2 v[126:127], v[122:123], off
	global_load_dwordx2 v[114:115], v[120:121], off offset:512
	global_load_dwordx2 v[116:117], v[122:123], off offset:512
	global_load_dwordx2 v[110:111], v[120:121], off offset:1024
	global_load_dwordx2 v[112:113], v[122:123], off offset:1024
	s_nop 0
	global_load_dwordx2 v[120:121], v[120:121], off offset:1536
	s_nop 0
	global_load_dwordx2 v[122:123], v[122:123], off offset:1536
	v_mov_b32_e32 v178, v161
	v_mov_b32_e32 v179, v163
	s_waitcnt lgkmcnt(0)
	v_add_f32_e32 v67, v67, v68
	v_fmamk_f32 v67, v67, 0x3a800000, v254
	v_rsq_f32_e32 v138, v67
	ds_swizzle_b32 v67, v66 offset:swizzle(SWAP,16)
	v_mov_b32_e32 v161, v162
	s_ashr_i32 s13, s12, 31
	v_pk_mul_f32 v[178:179], v[138:139], v[178:179] op_sel_hi:[0,1]
	v_pk_mul_f32 v[160:161], v[138:139], v[160:161] op_sel_hi:[0,1]
	s_waitcnt lgkmcnt(0)
	v_add_f32_e32 v66, v66, v67
	ds_bpermute_b32 v67, v79, v66
	s_lshl_b64 s[28:29], s[12:13], 10
	s_add_i32 s12, s12, 1
	s_ashr_i32 s13, s12, 31
	s_lshl_b64 s[12:13], s[12:13], 10
	s_waitcnt lgkmcnt(0)
	v_add_f32_e32 v66, v66, v67
	v_fmamk_f32 v66, v66, 0x3a800000, v254
	v_rsq_f32_e32 v140, v66
	v_mov_b64_e32 v[70:71], v[192:193]
	v_mov_b64_e32 v[72:73], v[194:195]
	v_mov_b64_e32 v[66:67], v[208:209]
	v_mov_b64_e32 v[68:69], v[210:211]
	v_mov_b64_e32 v[74:75], v[212:213]
	v_mov_b64_e32 v[76:77], v[214:215]
	v_pk_mul_f32 v[142:143], v[142:143], v[138:139] op_sel_hi:[1,0]
	v_pk_mul_f32 v[146:147], v[146:147], v[138:139] op_sel_hi:[1,0]
	v_pk_mul_f32 v[136:137], v[136:137], v[140:141] op_sel_hi:[1,0]
	v_pk_mul_f32 v[144:145], v[144:145], v[140:141] op_sel_hi:[1,0]
	v_pk_mul_f32 v[134:135], v[134:135], v[138:139] op_sel_hi:[1,0]
	v_pk_mul_f32 v[130:131], v[130:131], v[140:141] op_sel_hi:[1,0]
	s_nop 0
	v_pk_mul_f32 v[162:163], v[72:73], v[178:179]
	v_mov_b32_e32 v178, v157
	v_mov_b32_e32 v157, v158
	v_pk_mul_f32 v[156:157], v[140:141], v[156:157] op_sel_hi:[0,1]
	v_pk_mul_f32 v[160:161], v[70:71], v[160:161]
	s_nop 0
	v_pk_add_f32 v[74:75], v[74:75], 1.0 op_sel_hi:[1,0]
	v_pk_mul_f32 v[70:71], v[70:71], v[156:157]
	v_pk_fma_f32 v[160:161], v[160:161], v[74:75], v[66:67]
	v_pk_fma_f32 v[70:71], v[74:75], v[70:71], v[66:67]
	v_mov_b32_e32 v66, v1
	v_cvt_pk_fp8_f32 v66, v160, v161
	v_mov_b32_e32 v74, v1
	v_mov_b32_e32 v179, v159
	v_cvt_pk_fp8_f32 v74, v70, v71
	v_pk_add_f32 v[76:77], v[76:77], 1.0 op_sel_hi:[1,0]
	v_pk_mul_f32 v[178:179], v[140:141], v[178:179] op_sel_hi:[0,1]
	v_pk_fma_f32 v[162:163], v[162:163], v[76:77], v[68:69]
	v_pk_mul_f32 v[72:73], v[72:73], v[178:179]
	v_cvt_pk_fp8_f32 v66, v162, v163 op_sel:[0,0,1]
	v_pk_fma_f32 v[72:73], v[76:77], v[72:73], v[68:69]
	v_lshl_add_u64 v[68:69], v[86:87], 0, s[28:29]
	v_cvt_pk_fp8_f32 v74, v72, v73 op_sel:[0,0,1]
	global_store_dword v[68:69], v66, off
	v_lshl_add_u64 v[66:67], v[86:87], 0, s[12:13]
	v_cvt_pk_bf16_f32 v76, v160, s0
	global_store_dword v[66:67], v74, off
	v_cvt_pk_bf16_f32 v74, v160, v161
	v_lshlrev_b32_e32 v76, 16, v76
	v_and_b32_e32 v91, 0xffff0000, v74
	v_cvt_pk_bf16_f32 v77, v162, s0
	v_cvt_pk_bf16_f32 v75, v162, v163
	v_sub_f32_e32 v76, v160, v76
	v_sub_f32_e32 v91, v161, v91
	v_cvt_pk_bf16_f32 v76, v76, v91
	v_lshlrev_b32_e32 v77, 16, v77
	v_and_b32_e32 v91, 0xffff0000, v75
	v_sub_f32_e32 v77, v162, v77
	v_sub_f32_e32 v91, v163, v91
	v_cvt_pk_bf16_f32 v77, v77, v91
	v_cvt_pk_bf16_f32 v91, v70, s0
	v_cvt_pk_bf16_f32 v156, v70, v71
	v_lshlrev_b32_e32 v91, 16, v91
	v_sub_f32_e32 v70, v70, v91
	v_and_b32_e32 v91, 0xffff0000, v156
	v_cvt_pk_bf16_f32 v129, v72, s0
	v_sub_f32_e32 v71, v71, v91
	v_cvt_pk_bf16_f32 v157, v72, v73
	v_cvt_pk_bf16_f32 v70, v70, v71
	v_lshlrev_b32_e32 v71, 16, v129
	v_sub_f32_e32 v71, v72, v71
	v_and_b32_e32 v72, 0xffff0000, v157
	v_sub_f32_e32 v72, v73, v72
	v_add_u32_e32 v91, s46, v78
	v_cvt_pk_bf16_f32 v71, v71, v72
	ds_write_b64 v91, v[74:75]
	ds_write_b64 v91, v[76:77] offset:33024
	ds_write_b64 v91, v[156:157] offset:2064
	ds_write_b64 v91, v[70:71] offset:35088
	v_mov_b64_e32 v[70:71], v[196:197]
	v_mov_b64_e32 v[72:73], v[198:199]
	v_mov_b64_e32 v[74:75], v[216:217]
	v_mov_b64_e32 v[76:77], v[218:219]
	v_mov_b64_e32 v[156:157], v[220:221]
	v_mov_b64_e32 v[158:159], v[222:223]
	v_mov_b32_e32 v160, v153
	v_mov_b32_e32 v161, v155
	v_pk_mul_f32 v[160:161], v[138:139], v[160:161] op_sel_hi:[0,1]
	v_mov_b32_e32 v153, v154
	v_pk_mul_f32 v[152:153], v[138:139], v[152:153] op_sel_hi:[0,1]
	s_mov_b64 s[28:29], -1
	s_mov_b64 s[12:13], -1
	s_nop 0
	v_pk_mul_f32 v[154:155], v[160:161], v[72:73]
	v_mov_b32_e32 v160, v149
	v_mov_b32_e32 v149, v150
	v_pk_mul_f32 v[148:149], v[140:141], v[148:149] op_sel_hi:[0,1]
	v_pk_mul_f32 v[152:153], v[152:153], v[70:71]
	s_nop 0
	v_pk_add_f32 v[156:157], v[156:157], 1.0 op_sel_hi:[1,0]
	v_pk_mul_f32 v[70:71], v[148:149], v[70:71]
	v_pk_fma_f32 v[152:153], v[152:153], v[156:157], v[74:75]
	v_pk_fma_f32 v[70:71], v[70:71], v[156:157], v[74:75]
	v_mov_b32_e32 v74, v1
	v_cvt_pk_fp8_f32 v74, v152, v153
	v_pk_add_f32 v[158:159], v[158:159], 1.0 op_sel_hi:[1,0]
	v_mov_b32_e32 v161, v151
	v_pk_fma_f32 v[154:155], v[154:155], v[158:159], v[76:77]
	v_pk_mul_f32 v[160:161], v[140:141], v[160:161] op_sel_hi:[0,1]
	v_cvt_pk_fp8_f32 v74, v154, v155 op_sel:[0,0,1]
	v_pk_mul_f32 v[72:73], v[160:161], v[72:73]
	v_cvt_pk_bf16_f32 v75, v154, v155
	v_pk_fma_f32 v[72:73], v[72:73], v[158:159], v[76:77]
	global_store_dword v[68:69], v74, off offset:256
	v_mov_b32_e32 v74, v1
	v_cvt_pk_fp8_f32 v74, v70, v71
	v_cvt_pk_bf16_f32 v76, v152, s0
	v_lshlrev_b32_e32 v76, 16, v76
	v_cvt_pk_bf16_f32 v77, v154, s0
	v_cvt_pk_fp8_f32 v74, v72, v73 op_sel:[0,0,1]
	v_sub_f32_e32 v76, v152, v76
	v_lshlrev_b32_e32 v77, 16, v77
	v_sub_f32_e32 v77, v154, v77
	global_store_dword v[66:67], v74, off offset:256
	v_cvt_pk_bf16_f32 v74, v152, v153
	v_and_b32_e32 v129, 0xffff0000, v74
	v_sub_f32_e32 v129, v153, v129
	v_cvt_pk_bf16_f32 v76, v76, v129
	v_and_b32_e32 v129, 0xffff0000, v75
	v_sub_f32_e32 v129, v155, v129
	v_cvt_pk_bf16_f32 v77, v77, v129
	v_cvt_pk_bf16_f32 v129, v70, s0
	v_cvt_pk_bf16_f32 v148, v70, v71
	v_lshlrev_b32_e32 v129, 16, v129
	v_sub_f32_e32 v70, v70, v129
	v_and_b32_e32 v129, 0xffff0000, v148
	v_cvt_pk_bf16_f32 v133, v72, s0
	v_sub_f32_e32 v71, v71, v129
	v_cvt_pk_bf16_f32 v149, v72, v73
	v_cvt_pk_bf16_f32 v70, v70, v71
	v_lshlrev_b32_e32 v71, 16, v133
	v_sub_f32_e32 v71, v72, v71
	v_and_b32_e32 v72, 0xffff0000, v149
	v_sub_f32_e32 v72, v73, v72
	v_cvt_pk_bf16_f32 v71, v71, v72
	ds_write_b64 v177, v[74:75]
	ds_write_b64 v177, v[76:77] offset:33024
	ds_write_b64 v177, v[148:149] offset:2064
	ds_write_b64 v177, v[70:71] offset:35088
	v_mov_b64_e32 v[70:71], v[200:201]
	v_mov_b64_e32 v[72:73], v[202:203]
	v_mov_b64_e32 v[74:75], v[224:225]
	v_mov_b64_e32 v[76:77], v[226:227]
	v_mov_b64_e32 v[148:149], v[228:229]
	v_mov_b64_e32 v[150:151], v[230:231]
	s_nop 0
	v_pk_mul_f32 v[142:143], v[142:143], v[70:71]
	v_pk_mul_f32 v[70:71], v[136:137], v[70:71]
	s_nop 0
	v_pk_add_f32 v[148:149], v[148:149], 1.0 op_sel_hi:[1,0]
	v_pk_mul_f32 v[146:147], v[146:147], v[72:73]
	v_pk_fma_f32 v[142:143], v[142:143], v[148:149], v[74:75]
	v_pk_fma_f32 v[70:71], v[70:71], v[148:149], v[74:75]
	v_mov_b32_e32 v74, v1
	v_cvt_pk_fp8_f32 v74, v142, v143
	v_pk_add_f32 v[150:151], v[150:151], 1.0 op_sel_hi:[1,0]
	v_pk_mul_f32 v[72:73], v[144:145], v[72:73]
	v_pk_fma_f32 v[146:147], v[146:147], v[150:151], v[76:77]
	v_pk_fma_f32 v[72:73], v[72:73], v[150:151], v[76:77]
	v_cvt_pk_fp8_f32 v74, v146, v147 op_sel:[0,0,1]
	v_cvt_pk_bf16_f32 v76, v142, s0
	v_lshlrev_b32_e32 v76, 16, v76
	v_cvt_pk_bf16_f32 v77, v146, s0
	global_store_dword v[68:69], v74, off offset:512
	v_mov_b32_e32 v74, v1
	v_cvt_pk_fp8_f32 v74, v70, v71
	v_cvt_pk_bf16_f32 v75, v146, v147
	v_sub_f32_e32 v76, v142, v76
	v_lshlrev_b32_e32 v77, 16, v77
	v_cvt_pk_fp8_f32 v74, v72, v73 op_sel:[0,0,1]
	v_sub_f32_e32 v77, v146, v77
	v_cvt_pk_bf16_f32 v136, v70, v71
	v_cvt_pk_bf16_f32 v133, v72, s0
	global_store_dword v[66:67], v74, off offset:512
	v_cvt_pk_bf16_f32 v74, v142, v143
	v_and_b32_e32 v129, 0xffff0000, v74
	v_sub_f32_e32 v129, v143, v129
	v_cvt_pk_bf16_f32 v76, v76, v129
	v_and_b32_e32 v129, 0xffff0000, v75
	v_sub_f32_e32 v129, v147, v129
	v_cvt_pk_bf16_f32 v77, v77, v129
	v_cvt_pk_bf16_f32 v129, v70, s0
	v_lshlrev_b32_e32 v129, 16, v129
	v_sub_f32_e32 v70, v70, v129
	v_and_b32_e32 v129, 0xffff0000, v136
	v_sub_f32_e32 v71, v71, v129
	v_cvt_pk_bf16_f32 v137, v72, v73
	v_cvt_pk_bf16_f32 v70, v70, v71
	v_lshlrev_b32_e32 v71, 16, v133
	v_sub_f32_e32 v71, v72, v71
	v_and_b32_e32 v72, 0xffff0000, v137
	v_sub_f32_e32 v72, v73, v72
	v_cvt_pk_bf16_f32 v71, v71, v72
	ds_write_b64 v186, v[74:75]
	ds_write_b64 v186, v[76:77] offset:33024
	ds_write_b64 v186, v[136:137] offset:2064
	ds_write_b64 v186, v[70:71] offset:35088
	v_mov_b64_e32 v[70:71], v[204:205]
	v_mov_b64_e32 v[72:73], v[206:207]
	v_mov_b64_e32 v[142:143], v[232:233]
	v_mov_b64_e32 v[144:145], v[234:235]
	v_mov_b64_e32 v[74:75], v[236:237]
	v_mov_b64_e32 v[76:77], v[238:239]
	v_mov_b32_e32 v133, v125
	v_pk_mul_f32 v[132:133], v[132:133], v[138:139] op_sel_hi:[1,0]
	v_mov_b32_e32 v129, v93
	v_mov_b32_e32 v93, v1
	v_pk_mul_f32 v[128:129], v[128:129], v[140:141] op_sel_hi:[1,0]
	s_nop 0
	v_pk_mul_f32 v[132:133], v[132:133], v[70:71]
	v_pk_mul_f32 v[134:135], v[134:135], v[72:73]
	s_nop 0
	v_pk_add_f32 v[138:139], v[74:75], 1.0 op_sel_hi:[1,0]
	v_pk_add_f32 v[136:137], v[76:77], 1.0 op_sel_hi:[1,0]
	v_pk_fma_f32 v[76:77], v[132:133], v[138:139], v[142:143]
	v_pk_fma_f32 v[74:75], v[134:135], v[136:137], v[144:145]
	v_cvt_pk_fp8_f32 v93, v76, v77
	v_pk_mul_f32 v[128:129], v[128:129], v[70:71]
	v_pk_mul_f32 v[70:71], v[130:131], v[72:73]
	v_pk_fma_f32 v[72:73], v[128:129], v[138:139], v[142:143]
	v_cvt_pk_fp8_f32 v93, v74, v75 op_sel:[0,0,1]
	v_pk_fma_f32 v[70:71], v[70:71], v[136:137], v[144:145]
	global_store_dword v[68:69], v93, off offset:768
	v_mov_b32_e32 v68, v1
	v_cvt_pk_fp8_f32 v68, v72, v73
	v_cvt_pk_bf16_f32 v69, v74, s0
	v_lshlrev_b32_e32 v69, 16, v69
	v_sub_f32_e32 v69, v74, v69
	v_cvt_pk_fp8_f32 v68, v70, v71 op_sel:[0,0,1]
	global_store_dword v[66:67], v68, off offset:768
	v_cvt_pk_bf16_f32 v68, v76, s0
	v_cvt_pk_bf16_f32 v66, v76, v77
	v_lshlrev_b32_e32 v68, 16, v68
	v_cvt_pk_bf16_f32 v67, v74, v75
	v_sub_f32_e32 v68, v76, v68
	v_and_b32_e32 v76, 0xffff0000, v66
	v_sub_f32_e32 v76, v77, v76
	v_and_b32_e32 v74, 0xffff0000, v67
	v_cvt_pk_bf16_f32 v68, v68, v76
	v_sub_f32_e32 v74, v75, v74
	v_cvt_pk_bf16_f32 v76, v72, s0
	v_cvt_pk_bf16_f32 v69, v69, v74
	v_cvt_pk_bf16_f32 v74, v72, v73
	v_lshlrev_b32_e32 v76, 16, v76
	v_sub_f32_e32 v72, v72, v76
	v_and_b32_e32 v76, 0xffff0000, v74
	v_cvt_pk_bf16_f32 v77, v70, s0
	v_sub_f32_e32 v73, v73, v76
	v_cvt_pk_bf16_f32 v75, v70, v71
	v_cvt_pk_bf16_f32 v72, v72, v73
	v_lshlrev_b32_e32 v73, 16, v77
	v_sub_f32_e32 v70, v70, v73
	v_and_b32_e32 v73, 0xffff0000, v75
	v_sub_f32_e32 v71, v71, v73
	v_cvt_pk_bf16_f32 v73, v70, v71
	ds_write_b64 v187, v[66:67]
	ds_write_b64 v187, v[68:69] offset:33024
	ds_write_b64 v187, v[74:75] offset:2064
	ds_write_b64 v187, v[72:73] offset:35088
	s_waitcnt lgkmcnt(0)
	s_barrier
	ds_read_b128 v[66:69], v188
	ds_read_b128 v[70:73], v188 offset:33024
	s_waitcnt lgkmcnt(1)
	v_mfma_f32_16x16x32_bf16 v[74:77], v[66:69], v[58:61], 0
	v_mfma_f32_16x16x32_bf16 v[128:131], v[66:69], v[26:29], 0
	s_waitcnt lgkmcnt(0)
	v_mfma_f32_16x16x32_bf16 v[74:77], v[70:73], v[58:61], v[74:77]
	v_mfma_f32_16x16x32_bf16 v[70:73], v[70:73], v[26:29], v[128:131]
	v_mfma_f32_16x16x32_bf16 v[74:77], v[66:69], v[62:65], v[74:77]
	v_mfma_f32_16x16x32_bf16 v[66:69], v[66:69], v[30:33], v[70:73]
	s_nop 5
	ds_read_b128 v[70:73], v188 offset:64
	ds_read_b128 v[128:131], v188 offset:33088
	s_waitcnt lgkmcnt(1)
	v_mfma_f32_16x16x32_bf16 v[74:77], v[70:73], v[50:53], v[74:77]
	v_mfma_f32_16x16x32_bf16 v[66:69], v[70:73], v[18:21], v[66:69]
	s_waitcnt lgkmcnt(0)
	v_mfma_f32_16x16x32_bf16 v[74:77], v[128:131], v[50:53], v[74:77]
	v_mfma_f32_16x16x32_bf16 v[66:69], v[128:131], v[18:21], v[66:69]
	v_mfma_f32_16x16x32_bf16 v[74:77], v[70:73], v[54:57], v[74:77]
	v_mfma_f32_16x16x32_bf16 v[66:69], v[70:73], v[22:25], v[66:69]
	ds_read_b128 v[70:73], v188 offset:128
	ds_read_b128 v[128:131], v188 offset:33152
	s_waitcnt lgkmcnt(1)
	v_mfma_f32_16x16x32_bf16 v[74:77], v[70:73], v[42:45], v[74:77]
	v_mfma_f32_16x16x32_bf16 v[66:69], v[70:73], v[10:13], v[66:69]
	s_waitcnt lgkmcnt(0)
	v_mfma_f32_16x16x32_bf16 v[74:77], v[128:131], v[42:45], v[74:77]
	v_mfma_f32_16x16x32_bf16 v[66:69], v[128:131], v[10:13], v[66:69]
	v_mfma_f32_16x16x32_bf16 v[74:77], v[70:73], v[46:49], v[74:77]
	v_mfma_f32_16x16x32_bf16 v[66:69], v[70:73], v[14:17], v[66:69]
	ds_read_b128 v[70:73], v188 offset:192
	ds_read_b128 v[128:131], v188 offset:33216
	s_waitcnt lgkmcnt(1)
	v_mfma_f32_16x16x32_bf16 v[74:77], v[70:73], v[34:37], v[74:77]
	v_mfma_f32_16x16x32_bf16 v[66:69], v[70:73], v[2:5], v[66:69]
	s_waitcnt lgkmcnt(0)
	v_mfma_f32_16x16x32_bf16 v[74:77], v[128:131], v[34:37], v[74:77]
	v_mfma_f32_16x16x32_bf16 v[66:69], v[128:131], v[2:5], v[66:69]
	v_mfma_f32_16x16x32_bf16 v[74:77], v[70:73], v[38:41], v[74:77]
	v_mfma_f32_16x16x32_bf16 v[66:69], v[70:73], v[6:9], v[66:69]
	s_nop 7
	ds_write2_b32 v189, v74, v66 offset1:16
	ds_write2_b32 v189, v75, v67 offset0:32 offset1:48
	ds_write2_b32 v189, v76, v68 offset0:64 offset1:80
	ds_write2_b32 v189, v77, v69 offset0:96 offset1:112
	s_waitcnt lgkmcnt(0)
	s_barrier
	ds_read2st64_b32 v[66:67], v190 offset1:8
	s_waitcnt lgkmcnt(0)
	v_add_f32_e32 v66, v165, v66
	v_add_f32_e32 v68, v66, v67
	ds_read2st64_b32 v[66:67], v190 offset0:16 offset1:24
	s_waitcnt lgkmcnt(0)
	v_add_f32_e32 v66, v68, v66
	v_add_f32_e32 v68, v66, v67
	ds_read2st64_b32 v[66:67], v190 offset0:32 offset1:40
	s_waitcnt lgkmcnt(0)
	v_add_f32_e32 v66, v68, v66
	v_add_f32_e32 v68, v66, v67
	ds_read2st64_b32 v[66:67], v190 offset0:48 offset1:56
	s_waitcnt lgkmcnt(0)
	v_add_f32_e32 v66, v68, v66
	v_add_f32_e32 v69, v66, v67
	v_mov_b32_dpp v67, v164 quad_perm:[1,0,3,2] row_mask:0xf bank_mask:0xf bound_ctrl:1
	s_nop 0
	v_mov_b32_dpp v66, v69 quad_perm:[1,0,3,2] row_mask:0xf bank_mask:0xf bound_ctrl:1
	v_cmp_nlt_f32_e32 vcc, v69, v66
	s_and_saveexec_b64 s[30:31], vcc
	v_cmp_eq_f32_e32 vcc, v69, v66
	v_cmp_lt_i32_e64 s[12:13], v67, v164
	s_and_b64 s[12:13], vcc, s[12:13]
	s_orn2_b64 s[12:13], s[12:13], exec
	s_or_b64 exec, exec, s[30:31]
	v_cndmask_b32_e64 v66, v69, v66, s[12:13]
	v_cndmask_b32_e64 v67, v164, v67, s[12:13]
	s_nop 0
	v_mov_b32_dpp v68, v66 quad_perm:[2,3,0,1] row_mask:0xf bank_mask:0xf bound_ctrl:1
	v_mov_b32_dpp v70, v67 quad_perm:[2,3,0,1] row_mask:0xf bank_mask:0xf bound_ctrl:1
	v_cmp_nlt_f32_e32 vcc, v66, v68
	s_and_saveexec_b64 s[30:31], vcc
	v_cmp_eq_f32_e32 vcc, v66, v68
	v_cmp_lt_i32_e64 s[12:13], v70, v67
	s_and_b64 s[12:13], vcc, s[12:13]
	s_orn2_b64 s[28:29], s[12:13], exec
	s_or_b64 exec, exec, s[30:31]
	v_cndmask_b32_e64 v66, v66, v68, s[28:29]
	v_cndmask_b32_e64 v67, v67, v70, s[28:29]
	s_mov_b64 s[28:29], -1
	v_mov_b32_dpp v68, v66 row_half_mirror row_mask:0xf bank_mask:0xf bound_ctrl:1
	v_mov_b32_dpp v70, v67 row_half_mirror row_mask:0xf bank_mask:0xf bound_ctrl:1
	v_cmp_nlt_f32_e32 vcc, v66, v68
	s_mov_b64 s[12:13], -1
	s_and_saveexec_b64 s[30:31], vcc
	v_cmp_eq_f32_e32 vcc, v66, v68
	v_cmp_lt_i32_e64 s[12:13], v70, v67
	s_and_b64 s[12:13], vcc, s[12:13]
	s_orn2_b64 s[12:13], s[12:13], exec
	s_or_b64 exec, exec, s[30:31]
	v_cndmask_b32_e64 v68, v66, v68, s[12:13]
	v_cndmask_b32_e64 v66, v67, v70, s[12:13]
	s_nop 0
	v_mov_b32_dpp v67, v68 row_mirror row_mask:0xf bank_mask:0xf bound_ctrl:1
	v_mov_b32_dpp v70, v66 row_mirror row_mask:0xf bank_mask:0xf bound_ctrl:1
	v_cmp_nlt_f32_e32 vcc, v68, v67
	s_and_saveexec_b64 s[30:31], vcc
	v_cmp_eq_f32_e32 vcc, v68, v67
	v_cmp_lt_i32_e64 s[12:13], v70, v66
	s_and_b64 s[12:13], vcc, s[12:13]
	s_orn2_b64 s[28:29], s[12:13], exec
	s_or_b64 exec, exec, s[30:31]
	v_cndmask_b32_e64 v67, v68, v67, s[28:29]
	ds_swizzle_b32 v68, v67 offset:swizzle(SWAP,16)
	v_cndmask_b32_e64 v66, v66, v70, s[28:29]
	ds_swizzle_b32 v70, v66 offset:swizzle(SWAP,16)
	s_mov_b64 s[30:31], -1
	s_mov_b64 s[28:29], -1
	s_waitcnt lgkmcnt(1)
	v_cmp_nlt_f32_e32 vcc, v67, v68
	s_and_saveexec_b64 s[34:35], vcc
	s_cbranch_execz .LBB0_1066
	v_cmp_eq_f32_e32 vcc, v67, v68
	s_waitcnt lgkmcnt(0)
	v_cmp_lt_i32_e64 s[12:13], v70, v66
	s_and_b64 s[12:13], vcc, s[12:13]
	s_orn2_b64 s[28:29], s[12:13], exec

.LBB0_1098:
	s_or_b64 exec, exec, s[12:13]
	s_add_i32 s0, s0, 16
	v_add_u32_e32 v89, 0x100, v89
	s_cmpk_eq_i32 s0, 0x70
	v_add_u32_e32 v124, 64, v124
	s_cbranch_scc1 .LBB0_1100
	s_waitcnt vmcnt(8)
	v_mov_b64_e32 v[66:67], v[126:127]
	s_branch .LBB0_1056
.LBB0_1100:
	s_waitcnt vmcnt(8)
	v_and_b32_e32 v145, 0xffff0000, v118
	v_and_b32_e32 v149, 0xffff0000, v119
	v_lshlrev_b32_e32 v144, 16, v118
	v_lshlrev_b32_e32 v148, 16, v119
	v_mul_f32_e32 v66, v149, v149
	v_and_b32_e32 v137, 0xffff0000, v115
	v_and_b32_e32 v136, 0xffff0000, v114
	v_mul_f32_e32 v74, v145, v145
	v_lshlrev_b32_e32 v133, 16, v120
	v_pk_fma_f32 v[66:67], v[148:149], v[148:149], v[66:67] op_sel_hi:[1,1,0]
	v_lshlrev_b32_e32 v141, 16, v115
	v_lshlrev_b32_e32 v140, 16, v114
	v_pk_mul_f32 v[70:71], v[136:137], v[136:137]
	v_pk_fma_f32 v[74:75], v[144:145], v[144:145], v[74:75] op_sel_hi:[1,1,0]
	v_and_b32_e32 v131, 0xffff0000, v121
	v_lshlrev_b32_e32 v130, 16, v121
	v_and_b32_e32 v121, 0xffff0000, v120
	v_pk_fma_f32 v[70:71], v[140:141], v[140:141], v[70:71]
	v_mov_b32_e32 v132, v74
	v_mov_b32_e32 v76, v66
	v_mov_b32_e32 v77, v133
	v_mul_f32_e32 v89, v121, v121
	v_pk_add_f32 v[66:67], v[74:75], v[66:67]
	v_pk_mul_f32 v[74:75], v[132:133], v[76:77]
	v_pk_add_f32 v[70:71], v[70:71], v[70:71] op_sel:[0,1] op_sel_hi:[1,0]
	v_lshlrev_b32_e32 v146, 16, v127
	v_and_b32_e32 v147, 0xffff0000, v127
	v_and_b32_e32 v135, 0xffff0000, v117
	v_lshlrev_b32_e32 v139, 16, v117
	v_and_b32_e32 v117, 0xffff0000, v110
	v_and_b32_e32 v127, 0xffff0000, v111
	v_mov_b32_e32 v67, v75
	v_mov_b32_e32 v71, v89
	v_lshlrev_b32_e32 v142, 16, v126
	v_and_b32_e32 v143, 0xffff0000, v126
	v_and_b32_e32 v134, 0xffff0000, v116
	v_lshlrev_b32_e32 v138, 16, v116
	v_lshlrev_b32_e32 v116, 16, v110
	v_lshlrev_b32_e32 v126, 16, v111
	v_pk_add_f32 v[66:67], v[66:67], v[70:71]
	v_mul_f32_e32 v70, v117, v117
	v_mul_f32_e32 v74, v127, v127
	s_waitcnt lgkmcnt(0)
	v_mul_f32_e32 v93, v130, v130
	v_mul_f32_e32 v110, v131, v131
	v_pk_fma_f32 v[70:71], v[116:117], v[116:117], v[70:71] op_sel_hi:[1,1,0]
	v_pk_fma_f32 v[74:75], v[126:127], v[126:127], v[74:75] op_sel_hi:[1,1,0]
	v_mov_b32_e32 v71, v93
	v_mov_b32_e32 v75, v110
	v_pk_add_f32 v[70:71], v[70:71], v[74:75]
	v_mul_f32_e32 v68, v147, v147
	v_pk_add_f32 v[66:67], v[66:67], v[70:71]
	v_lshlrev_b32_e32 v129, 16, v122
	v_add_f32_e32 v74, v66, v67
	v_mul_f32_e32 v66, v143, v143
	v_pk_fma_f32 v[68:69], v[146:147], v[146:147], v[68:69] op_sel_hi:[1,1,0]
	v_pk_fma_f32 v[66:67], v[142:143], v[142:143], v[66:67] op_sel_hi:[1,1,0]
	v_pk_mul_f32 v[72:73], v[134:135], v[134:135]
	v_mov_b32_e32 v128, v66
	v_mov_b32_e32 v70, v68
	v_mov_b32_e32 v71, v129
	v_and_b32_e32 v125, 0xffff0000, v123
	v_lshlrev_b32_e32 v124, 16, v123
	v_and_b32_e32 v123, 0xffff0000, v122
	v_pk_fma_f32 v[72:73], v[138:139], v[138:139], v[72:73]
	v_pk_add_f32 v[66:67], v[66:67], v[68:69]
	v_pk_mul_f32 v[68:69], v[128:129], v[70:71]
	v_mul_f32_e32 v75, v123, v123
	v_mov_b32_e32 v67, v69
	v_pk_add_f32 v[68:69], v[72:73], v[72:73] op_sel:[0,1] op_sel_hi:[1,0]
	v_and_b32_e32 v115, 0xffff0000, v112
	v_and_b32_e32 v119, 0xffff0000, v113
	v_mov_b32_e32 v69, v75
	v_lshlrev_b32_e32 v114, 16, v112
	v_lshlrev_b32_e32 v118, 16, v113
	v_pk_add_f32 v[66:67], v[66:67], v[68:69]
	v_mul_f32_e32 v68, v115, v115
	v_mul_f32_e32 v70, v119, v119
	v_mul_f32_e32 v76, v124, v124
	v_mul_f32_e32 v77, v125, v125
	v_pk_fma_f32 v[68:69], v[114:115], v[114:115], v[68:69] op_sel_hi:[1,1,0]
	v_pk_fma_f32 v[70:71], v[118:119], v[118:119], v[70:71] op_sel_hi:[1,1,0]
	v_mov_b32_e32 v69, v76
	v_mov_b32_e32 v71, v77
	v_pk_add_f32 v[68:69], v[68:69], v[70:71]
	s_add_i32 s12, s26, 0x70
	v_pk_add_f32 v[66:67], v[66:67], v[68:69]
	s_ashr_i32 s13, s12, 31
	v_add_f32_e32 v66, v66, v67
	v_add_f32_dpp v67, v74, v74 quad_perm:[1,0,3,2] row_mask:0xf bank_mask:0xf bound_ctrl:1
	s_add_i32 s0, s26, 0x71
	v_add_f32_dpp v66, v66, v66 quad_perm:[1,0,3,2] row_mask:0xf bank_mask:0xf bound_ctrl:1
	v_add_f32_dpp v67, v67, v67 quad_perm:[2,3,0,1] row_mask:0xf bank_mask:0xf bound_ctrl:1
	s_lshl_b64 s[28:29], s[12:13], 10
	v_add_f32_dpp v66, v66, v66 quad_perm:[2,3,0,1] row_mask:0xf bank_mask:0xf bound_ctrl:1
	v_add_f32_dpp v67, v67, v67 row_half_mirror row_mask:0xf bank_mask:0xf bound_ctrl:1
	s_ashr_i32 s1, s0, 31
	v_add_f32_dpp v66, v66, v66 row_half_mirror row_mask:0xf bank_mask:0xf bound_ctrl:1
	v_add_f32_dpp v67, v67, v67 row_mirror row_mask:0xf bank_mask:0xf bound_ctrl:1
	ds_swizzle_b32 v68, v67 offset:swizzle(SWAP,16)
	v_add_f32_dpp v66, v66, v66 row_mirror row_mask:0xf bank_mask:0xf bound_ctrl:1
	s_lshl_b64 s[12:13], s[0:1], 10
	v_mov_b32_e32 v120, v133
	v_mov_b32_e32 v122, v129
	s_waitcnt lgkmcnt(0)
	v_add_f32_e32 v67, v67, v68
	ds_bpermute_b32 v68, v79, v67
	s_mov_b64 s[26:27], -1
	s_waitcnt lgkmcnt(0)
	v_add_f32_e32 v67, v67, v68
	v_fmamk_f32 v67, v67, 0x3a800000, v254
	v_rsq_f32_e32 v110, v67
	ds_swizzle_b32 v67, v66 offset:swizzle(SWAP,16)
	s_waitcnt lgkmcnt(0)
	v_add_f32_e32 v66, v66, v67
	ds_bpermute_b32 v67, v79, v66
	s_waitcnt lgkmcnt(0)
	v_add_f32_e32 v66, v66, v67
	v_fmamk_f32 v66, v66, 0x3a800000, v254
	v_rsq_f32_e32 v112, v66
	v_mov_b64_e32 v[70:71], v[192:193]
	v_mov_b64_e32 v[72:73], v[194:195]
	v_mov_b64_e32 v[66:67], v[208:209]
	v_mov_b64_e32 v[68:69], v[210:211]
	v_mov_b64_e32 v[74:75], v[212:213]
	v_mov_b64_e32 v[76:77], v[214:215]
	v_pk_mul_f32 v[108:109], v[110:111], v[144:145] op_sel_hi:[0,1]
	v_pk_mul_f32 v[106:107], v[110:111], v[148:149] op_sel_hi:[0,1]
	v_pk_mul_f32 v[142:143], v[112:113], v[142:143] op_sel_hi:[0,1]
	v_pk_mul_f32 v[144:145], v[112:113], v[146:147] op_sel_hi:[0,1]
	s_nop 0
	v_pk_mul_f32 v[108:109], v[70:71], v[108:109]
	v_pk_mul_f32 v[70:71], v[70:71], v[142:143]
	s_nop 0
	v_pk_add_f32 v[74:75], v[74:75], 1.0 op_sel_hi:[1,0]
	v_pk_mul_f32 v[106:107], v[72:73], v[106:107]
	v_pk_fma_f32 v[108:109], v[108:109], v[74:75], v[66:67]
	v_pk_fma_f32 v[70:71], v[74:75], v[70:71], v[66:67]
	v_mov_b32_e32 v66, v1
	v_cvt_pk_fp8_f32 v66, v108, v109
	v_mov_b32_e32 v74, v1
	v_cvt_pk_fp8_f32 v74, v70, v71
	v_pk_add_f32 v[76:77], v[76:77], 1.0 op_sel_hi:[1,0]
	v_pk_mul_f32 v[72:73], v[72:73], v[144:145]
	v_pk_fma_f32 v[106:107], v[106:107], v[76:77], v[68:69]
	v_pk_fma_f32 v[72:73], v[76:77], v[72:73], v[68:69]
	v_cvt_pk_fp8_f32 v66, v106, v107 op_sel:[0,0,1]
	v_cvt_pk_fp8_f32 v74, v72, v73 op_sel:[0,0,1]
	v_lshl_add_u64 v[68:69], v[86:87], 0, s[28:29]
	v_cvt_pk_bf16_f32 v76, v108, s0
	global_store_dword v[68:69], v66, off
	v_lshl_add_u64 v[66:67], v[86:87], 0, s[12:13]
	global_store_dword v[66:67], v74, off
	v_cvt_pk_bf16_f32 v74, v108, v109
	v_lshlrev_b32_e32 v76, 16, v76
	v_and_b32_e32 v89, 0xffff0000, v74
	v_cvt_pk_bf16_f32 v77, v106, s0
	v_cvt_pk_bf16_f32 v75, v106, v107
	v_sub_f32_e32 v76, v108, v76
	v_sub_f32_e32 v89, v109, v89
	v_cvt_pk_bf16_f32 v76, v76, v89
	v_lshlrev_b32_e32 v77, 16, v77
	v_and_b32_e32 v89, 0xffff0000, v75
	v_sub_f32_e32 v77, v106, v77
	v_sub_f32_e32 v89, v107, v89
	v_cvt_pk_bf16_f32 v77, v77, v89
	v_cvt_pk_bf16_f32 v89, v70, s0
	v_cvt_pk_bf16_f32 v106, v70, v71
	v_lshlrev_b32_e32 v89, 16, v89
	v_sub_f32_e32 v70, v70, v89
	v_and_b32_e32 v89, 0xffff0000, v106
	v_cvt_pk_bf16_f32 v93, v72, s0
	v_sub_f32_e32 v71, v71, v89
	v_cvt_pk_bf16_f32 v107, v72, v73
	v_cvt_pk_bf16_f32 v70, v70, v71
	v_lshlrev_b32_e32 v71, 16, v93
	v_sub_f32_e32 v71, v72, v71
	v_and_b32_e32 v72, 0xffff0000, v107
	v_sub_f32_e32 v72, v73, v72
	v_cvt_pk_bf16_f32 v71, v71, v72
	ds_write_b64 v91, v[74:75]
	ds_write_b64 v91, v[76:77] offset:33024
	ds_write_b64 v91, v[106:107] offset:2064
	ds_write_b64 v91, v[70:71] offset:35088
	v_mov_b64_e32 v[70:71], v[196:197]
	v_mov_b64_e32 v[72:73], v[198:199]
	v_mov_b64_e32 v[74:75], v[216:217]
	v_mov_b64_e32 v[76:77], v[218:219]
	s_nop 0
	v_mov_b64_e32 v[102:103], v[220:221]
	v_mov_b64_e32 v[104:105], v[222:223]
	v_mov_b32_e32 v106, v141
	v_mov_b32_e32 v141, v136
	v_mov_b32_e32 v136, v139
	v_mov_b32_e32 v139, v134
	v_mov_b32_e32 v107, v137
	v_pk_mul_f32 v[108:109], v[110:111], v[140:141] op_sel_hi:[0,1]
	v_mov_b32_e32 v137, v135
	v_pk_mul_f32 v[134:135], v[112:113], v[138:139] op_sel_hi:[0,1]
	v_pk_mul_f32 v[106:107], v[110:111], v[106:107] op_sel_hi:[0,1]
	v_pk_mul_f32 v[136:137], v[112:113], v[136:137] op_sel_hi:[0,1]
	s_mov_b64 s[12:13], -1
	s_nop 0
	v_pk_mul_f32 v[108:109], v[108:109], v[70:71]
	v_pk_mul_f32 v[70:71], v[134:135], v[70:71]
	s_nop 0
	v_pk_add_f32 v[102:103], v[102:103], 1.0 op_sel_hi:[1,0]
	v_pk_mul_f32 v[106:107], v[106:107], v[72:73]
	v_pk_fma_f32 v[108:109], v[108:109], v[102:103], v[74:75]
	v_pk_fma_f32 v[70:71], v[70:71], v[102:103], v[74:75]
	v_mov_b32_e32 v74, v1
	v_cvt_pk_fp8_f32 v74, v108, v109
	v_pk_add_f32 v[104:105], v[104:105], 1.0 op_sel_hi:[1,0]
	v_pk_mul_f32 v[72:73], v[136:137], v[72:73]
	v_pk_fma_f32 v[106:107], v[106:107], v[104:105], v[76:77]
	v_pk_fma_f32 v[72:73], v[72:73], v[104:105], v[76:77]
	v_cvt_pk_fp8_f32 v74, v106, v107 op_sel:[0,0,1]
	v_cvt_pk_bf16_f32 v76, v108, s0
	v_lshlrev_b32_e32 v76, 16, v76
	v_cvt_pk_bf16_f32 v77, v106, s0
	global_store_dword v[68:69], v74, off offset:256
	v_mov_b32_e32 v74, v1
	v_cvt_pk_fp8_f32 v74, v70, v71
	v_cvt_pk_bf16_f32 v75, v106, v107
	v_sub_f32_e32 v76, v108, v76
	v_lshlrev_b32_e32 v77, 16, v77
	v_cvt_pk_fp8_f32 v74, v72, v73 op_sel:[0,0,1]
	v_sub_f32_e32 v77, v106, v77
	v_cvt_pk_bf16_f32 v102, v70, v71
	v_cvt_pk_bf16_f32 v91, v72, s0
	global_store_dword v[66:67], v74, off offset:256
	v_cvt_pk_bf16_f32 v74, v108, v109
	v_and_b32_e32 v89, 0xffff0000, v74
	v_sub_f32_e32 v89, v109, v89
	v_cvt_pk_bf16_f32 v76, v76, v89
	v_and_b32_e32 v89, 0xffff0000, v75
	v_sub_f32_e32 v89, v107, v89
	v_cvt_pk_bf16_f32 v77, v77, v89
	v_cvt_pk_bf16_f32 v89, v70, s0
	v_lshlrev_b32_e32 v89, 16, v89
	v_sub_f32_e32 v70, v70, v89
	v_and_b32_e32 v89, 0xffff0000, v102
	v_sub_f32_e32 v71, v71, v89
	v_cvt_pk_bf16_f32 v103, v72, v73
	v_cvt_pk_bf16_f32 v70, v70, v71
	v_lshlrev_b32_e32 v71, 16, v91
	v_sub_f32_e32 v71, v72, v71
	v_and_b32_e32 v72, 0xffff0000, v103
	v_sub_f32_e32 v72, v73, v72
	v_cvt_pk_bf16_f32 v71, v71, v72
	ds_write_b64 v177, v[74:75]
	ds_write_b64 v177, v[76:77] offset:33024
	ds_write_b64 v177, v[102:103] offset:2064
	ds_write_b64 v177, v[70:71] offset:35088
	v_mov_b64_e32 v[70:71], v[200:201]
	v_mov_b64_e32 v[72:73], v[202:203]
	v_mov_b64_e32 v[74:75], v[224:225]
	v_mov_b64_e32 v[76:77], v[226:227]
	s_nop 0
	v_mov_b64_e32 v[98:99], v[228:229]
	v_mov_b64_e32 v[100:101], v[230:231]
	v_pk_mul_f32 v[104:105], v[110:111], v[116:117] op_sel_hi:[0,1]
	v_pk_mul_f32 v[108:109], v[112:113], v[114:115] op_sel_hi:[0,1]
	v_pk_mul_f32 v[102:103], v[110:111], v[126:127] op_sel_hi:[0,1]
	v_pk_mul_f32 v[106:107], v[112:113], v[118:119] op_sel_hi:[0,1]
	s_nop 0
	v_pk_mul_f32 v[104:105], v[104:105], v[70:71]
	v_pk_mul_f32 v[70:71], v[108:109], v[70:71]
	s_nop 0
	v_pk_add_f32 v[98:99], v[98:99], 1.0 op_sel_hi:[1,0]
	v_pk_mul_f32 v[102:103], v[102:103], v[72:73]
	v_pk_fma_f32 v[104:105], v[104:105], v[98:99], v[74:75]
	v_pk_fma_f32 v[70:71], v[70:71], v[98:99], v[74:75]
	v_mov_b32_e32 v74, v1
	v_cvt_pk_fp8_f32 v74, v104, v105
	v_pk_add_f32 v[100:101], v[100:101], 1.0 op_sel_hi:[1,0]
	v_pk_mul_f32 v[72:73], v[106:107], v[72:73]
	v_pk_fma_f32 v[102:103], v[102:103], v[100:101], v[76:77]
	v_pk_fma_f32 v[72:73], v[72:73], v[100:101], v[76:77]
	v_cvt_pk_fp8_f32 v74, v102, v103 op_sel:[0,0,1]
	v_cvt_pk_bf16_f32 v76, v104, s0
	v_lshlrev_b32_e32 v76, 16, v76
	v_cvt_pk_bf16_f32 v77, v102, s0
	global_store_dword v[68:69], v74, off offset:512
	v_mov_b32_e32 v74, v1
	v_cvt_pk_fp8_f32 v74, v70, v71
	v_cvt_pk_bf16_f32 v75, v102, v103
	v_sub_f32_e32 v76, v104, v76
	v_lshlrev_b32_e32 v77, 16, v77
	v_cvt_pk_fp8_f32 v74, v72, v73 op_sel:[0,0,1]
	v_sub_f32_e32 v77, v102, v77
	v_cvt_pk_bf16_f32 v98, v70, v71
	v_cvt_pk_bf16_f32 v91, v72, s0
	global_store_dword v[66:67], v74, off offset:512
	v_cvt_pk_bf16_f32 v74, v104, v105
	v_and_b32_e32 v89, 0xffff0000, v74
	v_sub_f32_e32 v89, v105, v89
	v_cvt_pk_bf16_f32 v76, v76, v89
	v_and_b32_e32 v89, 0xffff0000, v75
	v_sub_f32_e32 v89, v103, v89
	v_cvt_pk_bf16_f32 v77, v77, v89
	v_cvt_pk_bf16_f32 v89, v70, s0
	v_lshlrev_b32_e32 v89, 16, v89
	v_sub_f32_e32 v70, v70, v89
	v_and_b32_e32 v89, 0xffff0000, v98
	v_sub_f32_e32 v71, v71, v89
	v_cvt_pk_bf16_f32 v99, v72, v73
	v_cvt_pk_bf16_f32 v70, v70, v71
	v_lshlrev_b32_e32 v71, 16, v91
	v_sub_f32_e32 v71, v72, v71
	v_and_b32_e32 v72, 0xffff0000, v99
	v_sub_f32_e32 v72, v73, v72
	v_cvt_pk_bf16_f32 v71, v71, v72
	ds_write_b64 v186, v[74:75]
	ds_write_b64 v186, v[76:77] offset:33024
	ds_write_b64 v186, v[98:99] offset:2064
	ds_write_b64 v186, v[70:71] offset:35088
	v_mov_b64_e32 v[70:71], v[204:205]
	v_mov_b64_e32 v[72:73], v[206:207]
	v_mov_b64_e32 v[98:99], v[232:233]
	v_mov_b64_e32 v[100:101], v[234:235]
	v_mov_b64_e32 v[74:75], v[236:237]
	v_mov_b64_e32 v[76:77], v[238:239]
	v_pk_mul_f32 v[96:97], v[120:121], v[110:111] op_sel_hi:[1,0]
	v_mov_b32_e32 v89, v1
	v_pk_mul_f32 v[94:95], v[130:131], v[110:111] op_sel_hi:[1,0]
	s_nop 0
	v_pk_mul_f32 v[96:97], v[96:97], v[70:71]
	v_pk_mul_f32 v[94:95], v[94:95], v[72:73]
	s_nop 0
	v_pk_add_f32 v[104:105], v[74:75], 1.0 op_sel_hi:[1,0]
	v_pk_add_f32 v[102:103], v[76:77], 1.0 op_sel_hi:[1,0]
	v_pk_fma_f32 v[76:77], v[96:97], v[104:105], v[98:99]
	v_pk_fma_f32 v[74:75], v[94:95], v[102:103], v[100:101]
	v_cvt_pk_fp8_f32 v89, v76, v77
	v_pk_mul_f32 v[96:97], v[122:123], v[112:113] op_sel_hi:[1,0]
	v_pk_mul_f32 v[94:95], v[124:125], v[112:113] op_sel_hi:[1,0]
	v_pk_mul_f32 v[96:97], v[96:97], v[70:71]
	v_cvt_pk_fp8_f32 v89, v74, v75 op_sel:[0,0,1]
	v_pk_mul_f32 v[70:71], v[94:95], v[72:73]
	v_pk_fma_f32 v[72:73], v[96:97], v[104:105], v[98:99]
	v_pk_fma_f32 v[70:71], v[70:71], v[102:103], v[100:101]
	global_store_dword v[68:69], v89, off offset:768
	v_mov_b32_e32 v68, v1
	v_cvt_pk_fp8_f32 v68, v72, v73
	v_cvt_pk_bf16_f32 v69, v74, s0
	v_lshlrev_b32_e32 v69, 16, v69
	v_sub_f32_e32 v69, v74, v69
	v_cvt_pk_fp8_f32 v68, v70, v71 op_sel:[0,0,1]
	global_store_dword v[66:67], v68, off offset:768
	v_cvt_pk_bf16_f32 v68, v76, s0
	v_cvt_pk_bf16_f32 v66, v76, v77
	v_lshlrev_b32_e32 v68, 16, v68
	v_cvt_pk_bf16_f32 v67, v74, v75
	v_sub_f32_e32 v68, v76, v68
	v_and_b32_e32 v76, 0xffff0000, v66
	v_sub_f32_e32 v76, v77, v76
	v_and_b32_e32 v74, 0xffff0000, v67
	v_cvt_pk_bf16_f32 v68, v68, v76
	v_sub_f32_e32 v74, v75, v74
	v_cvt_pk_bf16_f32 v76, v72, s0
	v_cvt_pk_bf16_f32 v69, v69, v74
	v_cvt_pk_bf16_f32 v74, v72, v73
	v_lshlrev_b32_e32 v76, 16, v76
	v_sub_f32_e32 v72, v72, v76
	v_and_b32_e32 v76, 0xffff0000, v74
	v_cvt_pk_bf16_f32 v77, v70, s0
	v_sub_f32_e32 v73, v73, v76
	v_cvt_pk_bf16_f32 v75, v70, v71
	v_cvt_pk_bf16_f32 v72, v72, v73
	v_lshlrev_b32_e32 v73, 16, v77
	v_sub_f32_e32 v70, v70, v73
	v_and_b32_e32 v73, 0xffff0000, v75
	v_sub_f32_e32 v71, v71, v73
	v_cvt_pk_bf16_f32 v73, v70, v71
	ds_write_b64 v187, v[66:67]
	ds_write_b64 v187, v[68:69] offset:33024
	ds_write_b64 v187, v[74:75] offset:2064
	ds_write_b64 v187, v[72:73] offset:35088
	s_waitcnt lgkmcnt(0)
	s_barrier
	ds_read_b128 v[66:69], v188
	ds_read_b128 v[70:73], v188 offset:33024
	s_waitcnt lgkmcnt(1)
	v_mfma_f32_16x16x32_bf16 v[74:77], v[66:69], v[58:61], 0
	v_mfma_f32_16x16x32_bf16 v[94:97], v[66:69], v[26:29], 0
	s_waitcnt lgkmcnt(0)
	v_mfma_f32_16x16x32_bf16 v[74:77], v[70:73], v[58:61], v[74:77]
	v_mfma_f32_16x16x32_bf16 v[70:73], v[70:73], v[26:29], v[94:97]
	v_mfma_f32_16x16x32_bf16 v[74:77], v[66:69], v[62:65], v[74:77]
	v_mfma_f32_16x16x32_bf16 v[66:69], v[66:69], v[30:33], v[70:73]
	s_nop 5
	ds_read_b128 v[70:73], v188 offset:64
	ds_read_b128 v[94:97], v188 offset:33088
	s_waitcnt lgkmcnt(1)
	v_mfma_f32_16x16x32_bf16 v[74:77], v[70:73], v[50:53], v[74:77]
	v_mfma_f32_16x16x32_bf16 v[66:69], v[70:73], v[18:21], v[66:69]
	s_waitcnt lgkmcnt(0)
	v_mfma_f32_16x16x32_bf16 v[74:77], v[94:97], v[50:53], v[74:77]
	v_mfma_f32_16x16x32_bf16 v[66:69], v[94:97], v[18:21], v[66:69]
	v_mfma_f32_16x16x32_bf16 v[74:77], v[70:73], v[54:57], v[74:77]
	v_mfma_f32_16x16x32_bf16 v[66:69], v[70:73], v[22:25], v[66:69]
	ds_read_b128 v[70:73], v188 offset:128
	ds_read_b128 v[94:97], v188 offset:33152
	s_waitcnt lgkmcnt(1)
	v_mfma_f32_16x16x32_bf16 v[74:77], v[70:73], v[42:45], v[74:77]
	v_mfma_f32_16x16x32_bf16 v[66:69], v[70:73], v[10:13], v[66:69]
	s_waitcnt lgkmcnt(0)
	v_mfma_f32_16x16x32_bf16 v[74:77], v[94:97], v[42:45], v[74:77]
	v_mfma_f32_16x16x32_bf16 v[66:69], v[94:97], v[10:13], v[66:69]
	v_mfma_f32_16x16x32_bf16 v[74:77], v[70:73], v[46:49], v[74:77]
	v_mfma_f32_16x16x32_bf16 v[66:69], v[70:73], v[14:17], v[66:69]
	ds_read_b128 v[70:73], v188 offset:192
	ds_read_b128 v[94:97], v188 offset:33216
	s_waitcnt lgkmcnt(1)
	v_mfma_f32_16x16x32_bf16 v[74:77], v[70:73], v[34:37], v[74:77]
	v_mfma_f32_16x16x32_bf16 v[66:69], v[70:73], v[2:5], v[66:69]
	s_waitcnt lgkmcnt(0)
	v_mfma_f32_16x16x32_bf16 v[74:77], v[94:97], v[34:37], v[74:77]
	v_mfma_f32_16x16x32_bf16 v[66:69], v[94:97], v[2:5], v[66:69]
	v_mfma_f32_16x16x32_bf16 v[74:77], v[70:73], v[38:41], v[74:77]
	v_mfma_f32_16x16x32_bf16 v[66:69], v[70:73], v[6:9], v[66:69]
	s_nop 7
	ds_write2_b32 v189, v74, v66 offset1:16
	ds_write2_b32 v189, v75, v67 offset0:32 offset1:48
	ds_write2_b32 v189, v76, v68 offset0:64 offset1:80
	ds_write2_b32 v189, v77, v69 offset0:96 offset1:112
	s_waitcnt lgkmcnt(0)
	s_barrier
	ds_read2st64_b32 v[66:67], v190 offset1:8
	s_waitcnt lgkmcnt(0)
	v_add_f32_e32 v66, v165, v66
	v_add_f32_e32 v68, v66, v67
	ds_read2st64_b32 v[66:67], v190 offset0:16 offset1:24
	s_waitcnt lgkmcnt(0)
	v_add_f32_e32 v66, v68, v66
	v_add_f32_e32 v68, v66, v67
	ds_read2st64_b32 v[66:67], v190 offset0:32 offset1:40
	s_waitcnt lgkmcnt(0)
	v_add_f32_e32 v66, v68, v66
	v_add_f32_e32 v68, v66, v67
	ds_read2st64_b32 v[66:67], v190 offset0:48 offset1:56
	s_waitcnt lgkmcnt(0)
	v_add_f32_e32 v66, v68, v66
	v_add_f32_e32 v69, v66, v67
	v_mov_b32_dpp v67, v164 quad_perm:[1,0,3,2] row_mask:0xf bank_mask:0xf bound_ctrl:1
	s_nop 0
	v_mov_b32_dpp v66, v69 quad_perm:[1,0,3,2] row_mask:0xf bank_mask:0xf bound_ctrl:1
	v_cmp_nlt_f32_e32 vcc, v69, v66
	s_and_saveexec_b64 s[28:29], vcc
	v_cmp_eq_f32_e32 vcc, v69, v66
	v_cmp_lt_i32_e64 s[12:13], v67, v164
	s_and_b64 s[0:1], vcc, s[12:13]
	s_orn2_b64 s[12:13], s[0:1], exec
	s_or_b64 exec, exec, s[28:29]
	v_cndmask_b32_e64 v66, v69, v66, s[12:13]
	v_cndmask_b32_e64 v67, v164, v67, s[12:13]
	s_nop 0
	v_mov_b32_dpp v68, v66 quad_perm:[2,3,0,1] row_mask:0xf bank_mask:0xf bound_ctrl:1
	v_mov_b32_dpp v70, v67 quad_perm:[2,3,0,1] row_mask:0xf bank_mask:0xf bound_ctrl:1
	v_cmp_nlt_f32_e32 vcc, v66, v68
	s_and_saveexec_b64 s[28:29], vcc
	v_cmp_eq_f32_e32 vcc, v66, v68
	v_cmp_lt_i32_e64 s[12:13], v70, v67
	s_and_b64 s[0:1], vcc, s[12:13]
	s_orn2_b64 s[26:27], s[0:1], exec
	s_or_b64 exec, exec, s[28:29]
	v_cndmask_b32_e64 v66, v66, v68, s[26:27]
	v_cndmask_b32_e64 v67, v67, v70, s[26:27]
	s_mov_b64 s[26:27], -1
	v_mov_b32_dpp v68, v66 row_half_mirror row_mask:0xf bank_mask:0xf bound_ctrl:1
	v_mov_b32_dpp v70, v67 row_half_mirror row_mask:0xf bank_mask:0xf bound_ctrl:1
	v_cmp_nlt_f32_e32 vcc, v66, v68
	s_mov_b64 s[12:13], -1
	s_and_saveexec_b64 s[28:29], vcc
	v_cmp_eq_f32_e32 vcc, v66, v68
	v_cmp_lt_i32_e64 s[12:13], v70, v67
	s_and_b64 s[0:1], vcc, s[12:13]
	s_orn2_b64 s[12:13], s[0:1], exec
	s_or_b64 exec, exec, s[28:29]
	v_cndmask_b32_e64 v68, v66, v68, s[12:13]
	v_cndmask_b32_e64 v66, v67, v70, s[12:13]
	s_nop 0
	v_mov_b32_dpp v67, v68 row_mirror row_mask:0xf bank_mask:0xf bound_ctrl:1
	v_mov_b32_dpp v70, v66 row_mirror row_mask:0xf bank_mask:0xf bound_ctrl:1
	v_cmp_nlt_f32_e32 vcc, v68, v67
	s_and_saveexec_b64 s[28:29], vcc
	v_cmp_eq_f32_e32 vcc, v68, v67
	v_cmp_lt_i32_e64 s[12:13], v70, v66
	s_and_b64 s[0:1], vcc, s[12:13]
	s_orn2_b64 s[26:27], s[0:1], exec
	s_or_b64 exec, exec, s[28:29]
	v_cndmask_b32_e64 v67, v68, v67, s[26:27]
	ds_swizzle_b32 v68, v67 offset:swizzle(SWAP,16)
	v_cndmask_b32_e64 v66, v66, v70, s[26:27]
	ds_swizzle_b32 v70, v66 offset:swizzle(SWAP,16)
	s_mov_b64 s[28:29], -1
	s_mov_b64 s[26:27], -1
	s_waitcnt lgkmcnt(1)
	v_cmp_nlt_f32_e32 vcc, v67, v68
	s_and_saveexec_b64 s[30:31], vcc
	s_cbranch_execz .LBB0_1110
	v_cmp_eq_f32_e32 vcc, v67, v68
	s_waitcnt lgkmcnt(0)
	v_cmp_lt_i32_e64 s[12:13], v70, v66
	s_and_b64 s[0:1], vcc, s[12:13]
	s_orn2_b64 s[26:27], s[0:1], exec
